# FoX unit: Q loads overlap the first pruning loads
# baseline (speedup 1.0000x reference)
.LBB0_479:
	s_or_b64 exec, exec, s[2:3]
	s_waitcnt lgkmcnt(0)
	s_barrier
	ds_read_b32 v1, v205
	s_mov_b64 s[2:3], -1
	s_waitcnt lgkmcnt(0)
	v_cmp_le_i32_e32 vcc, s29, v1
	v_readfirstlane_b32 s4, v1
	s_cbranch_vccnz .LBB0_474
	s_add_i32 s2, s4, 0xfffffe00
	s_cmpk_gt_i32 s4, 0x1ff
	s_cselect_b32 s2, s2, s4
	s_ashr_i32 s3, s2, 31
	s_lshr_b32 s3, s3, 26
	s_add_i32 s3, s2, s3
	s_ashr_i32 s52, s3, 6
	s_andn2_b32 s3, s3, 63
	s_sub_i32 s2, s2, s3
	v_mov_b32_e32 v1, v0
	s_ashr_i32 s20, s2, 2
	s_lshl_b32 s2, s2, 1
	v_readfirstlane_b32 s56, v1
	s_ashr_i32 s50, s56, 6
	s_ashr_i32 s51, s56, 8
	s_and_b32 s55, s2, 6
	s_sub_i32 s54, 7, s52
	s_and_b32 s53, s50, 3
	s_add_i32 s3, s51, s55
	s_ashr_i32 s21, s20, 31
	s_lshl_b32 s2, s54, 8
	s_lshl_b32 s57, s53, 6
	s_lshl_b32 s18, s3, 6
	s_or_b32 s6, s57, s2
	s_lshl_b64 s[4:5], s[20:21], 20
	s_ashr_i32 s19, s18, 31
	s_add_u32 s4, s4, s18
	v_and_b32_e32 v230, 31, v1
	s_addc_u32 s5, s5, s19
	v_or_b32_e32 v2, s6, v230
	s_lshl_b64 s[22:23], s[4:5], 1
	v_or_b32_e32 v4, 32, v2
	s_add_u32 s4, s30, s22
	v_mov_b32_e32 v5, v3
	s_addc_u32 s5, s31, s23
	v_lshlrev_b64 v[6:7], 10, v[2:3]
	v_lshlrev_b64 v[4:5], 10, v[4:5]
	s_lshl_b32 s58, s20, 3
	v_lshl_add_u64 v[6:7], s[4:5], 0, v[6:7]
	v_lshl_add_u64 v[4:5], s[4:5], 0, v[4:5]
	s_add_i32 s4, s3, s58
	s_ashr_i32 s5, s4, 31
	v_bfe_u32 v229, v1, 5, 1
	s_lshl_b64 s[4:5], s[4:5], 13
	v_lshlrev_b32_e32 v8, 4, v229
	v_mov_b32_e32 v9, v3
	s_add_u32 s4, s33, s4
	v_lshl_add_u64 v[4:5], v[4:5], 0, v[8:9]
	s_addc_u32 s5, s34, s5
	v_lshl_add_u64 v[6:7], v[6:7], 0, v[8:9]
	v_lshl_add_u64 v[8:9], v[2:3], 2, s[4:5]
	global_load_dwordx4 v[162:165], v[4:5], off offset:96
	global_load_dwordx4 v[166:169], v[4:5], off offset:64
	global_load_dwordx4 v[170:173], v[6:7], off offset:96
	global_load_dwordx4 v[174:177], v[6:7], off offset:64
	global_load_dwordx4 v[178:181], v[4:5], off offset:32
	global_load_dwordx4 v[182:185], v[4:5], off
	global_load_dwordx4 v[186:189], v[6:7], off offset:32
	global_load_dwordx4 v[190:193], v[6:7], off
	global_load_dword v232, v[8:9], off offset:128
	global_load_dword v233, v[8:9], off
	s_or_b32 s24, s55, s58
	s_ashr_i32 s25, s24, 31
	s_add_i32 s59, s58, 0x80
	s_lshl_b64 s[26:27], s[24:25], 13
	s_add_u32 s26, s33, s26
	s_addc_u32 s27, s34, s27
	s_lshl_b64 s[60:61], s[24:25], 2
	s_add_u32 s60, s35, s60
	s_mov_b32 s5, s7
	s_addc_u32 s61, s38, s61
	s_or_b32 s4, s59, s55
	v_mov_b32_e32 v2, v3
	v_mov_b32_e32 v4, v3
	s_lshl_b64 s[4:5], s[4:5], 2
	s_add_u32 s4, s35, s4
	s_addc_u32 s5, s38, s5
	s_mov_b32 s3, s7
	v_lshlrev_b32_e32 v5, 8, v230
	v_mov_b32_e32 v234, 0
	global_load_dword v2, v3, s[60:61]
	global_load_dword v4, v3, s[4:5]
	s_lshl_b64 s[4:5], s[2:3], 2
	s_add_u32 s2, s26, s4
	s_addc_u32 s3, s27, s5
	global_load_dword v6, v3, s[2:3]
	s_nop 0
	global_load_dword v5, v5, s[26:27] offset:252
	s_cmpk_gt_u32 s56, 0xff
	s_waitcnt vmcnt(2)
	v_mul_f32_e32 v2, v2, v4
	v_mul_f32_e32 v4, 0x4f800000, v2
	v_cmp_gt_f32_e32 vcc, s44, v2
	s_waitcnt vmcnt(0)
	v_sub_f32_e32 v5, v6, v5
	v_cndmask_b32_e32 v2, v2, v4, vcc
	v_sqrt_f32_e32 v4, v2
	s_nop 0
	v_add_u32_e32 v6, -1, v4
	v_add_u32_e32 v7, 1, v4
	v_fma_f32 v8, -v6, v4, v2
	v_fma_f32 v9, -v7, v4, v2
	v_cmp_ge_f32_e64 s[2:3], 0, v8
	s_nop 1
	v_cndmask_b32_e64 v4, v4, v6, s[2:3]
	v_cmp_lt_f32_e64 s[2:3], 0, v9
	s_nop 1
	v_cndmask_b32_e64 v4, v4, v7, s[2:3]
	v_mul_f32_e32 v6, 0x37800000, v4
	v_cndmask_b32_e32 v4, v4, v6, vcc
	v_cmp_class_f32_e32 vcc, v2, v226
	s_nop 1
	v_cndmask_b32_e32 v2, v4, v2, vcc
	v_fmac_f32_e32 v5, 2.0, v2
	v_cmp_le_f32_e32 vcc, s45, v5
	s_cbranch_scc1 .LBB0_482
	s_lshl_b64 s[2:3], s[6:7], 2
	s_add_u32 s2, s26, s2
	s_addc_u32 s3, s27, s3
	global_load_dword v4, v3, s[2:3]
	v_add_f32_e32 v2, v2, v2
	v_add_f32_e32 v2, 0x42480000, v2
	s_waitcnt vmcnt(0)
	v_add_f32_e32 v234, v2, v4
